# speedup vs baseline: 1.1288x; 1.0126x over previous
.LBB2_27:
	ds_read2st64_b32 v[10:11], v8 offset1:1
	v_add_u32_e32 v7, 16, v7
	v_cmp_lt_u32_e32 vcc, 3, v7
	s_or_b64 s[0:1], vcc, s[0:1]
	s_waitcnt lgkmcnt(0)
	v_max_f32_e32 v9, v11, v11
	v_max_f32_e32 v12, v10, v10
	v_max_f32_e32 v9, v12, v9
	s_nop 1
	v_max_f32_dpp v9, v9, v9 quad_perm:[1,0,3,2] row_mask:0xf bank_mask:0xf
	s_nop 1
	v_max_f32_dpp v9, v9, v9 quad_perm:[2,3,0,1] row_mask:0xf bank_mask:0xf
	s_nop 1
	v_max_f32_dpp v9, v9, v9 row_half_mirror row_mask:0xf bank_mask:0xf
	s_nop 1
	v_max_f32_dpp v9, v9, v9 row_mirror row_mask:0xf bank_mask:0xf
	s_nop 1
	v_readlane_b32 s30, v9, 0
	v_readlane_b32 s31, v9, 16
	v_readlane_b32 s32, v9, 32
	v_readlane_b32 s33, v9, 48
	v_mov_b32_e32 v9, s30
	v_max_f32_e32 v9, s31, v9
	v_max_f32_e32 v9, s32, v9
	v_max_f32_e32 v9, s33, v9
	v_sub_f32_e32 v10, v10, v9
	v_sub_f32_e32 v9, v11, v9
	v_mul_f32_e32 v10, 0x3fb8aa3b, v10
	v_mul_f32_e32 v9, 0x3fb8aa3b, v9
	v_exp_f32_e32 v10, v10
	v_exp_f32_e32 v9, v9
	s_nop 0
	v_add_f32_e32 v11, v10, v9
	s_nop 1
	v_add_f32_dpp v11, v11, v11 quad_perm:[1,0,3,2] row_mask:0xf bank_mask:0xf
	s_nop 1
	v_add_f32_dpp v11, v11, v11 quad_perm:[2,3,0,1] row_mask:0xf bank_mask:0xf
	s_nop 1
	v_add_f32_dpp v11, v11, v11 row_half_mirror row_mask:0xf bank_mask:0xf
	s_nop 1
	v_add_f32_dpp v11, v11, v11 row_mirror row_mask:0xf bank_mask:0xf
	s_nop 1
	v_readlane_b32 s30, v11, 0
	v_readlane_b32 s31, v11, 16
	v_readlane_b32 s32, v11, 32
	v_readlane_b32 s33, v11, 48
	v_mov_b32_e32 v11, s30
	v_add_f32_e32 v11, s31, v11
	v_add_f32_e32 v11, s32, v11
	v_add_f32_e32 v11, s33, v11
	v_div_scale_f32 v12, s[4:5], v11, v11, 1.0
	v_rcp_f32_e32 v13, v12
	v_div_scale_f32 v14, vcc, 1.0, v11, 1.0
	v_fma_f32 v15, -v12, v13, 1.0
	v_fmac_f32_e32 v13, v15, v13
	v_mul_f32_e32 v15, v14, v13
	v_fma_f32 v16, -v12, v15, v14
	v_fmac_f32_e32 v15, v16, v13
	v_fma_f32 v12, -v12, v15, v14
	v_div_fmas_f32 v12, v12, v13, v15
	v_div_fixup_f32 v11, v12, v11, 1.0
	v_mul_f32_e32 v10, v10, v11
	v_mul_f32_e32 v9, v9, v11
	ds_write2st64_b32 v8, v10, v9 offset1:1
	v_add_u32_e32 v8, 0x2000, v8
	s_andn2_b64 exec, exec, s[0:1]
	s_cbranch_execnz .LBB2_27
	s_or_b64 exec, exec, s[0:1]
	v_and_b32_e32 v2, 0x1ff, v0
	s_movk_i32 s4, 0x176
	v_mul_u32_u24_e32 v1, 0x36a, v2
	v_lshrrev_b32_e32 v72, 16, v1
	v_cmp_lt_u32_e32 vcc, s4, v2
	s_movk_i32 s0, 0x177
	s_movk_i32 s4, 0xffb5
	v_cndmask_b32_e64 v1, v72, 0, vcc
	v_mov_b32_e32 v9, 0
	s_movk_i32 s10, 0x1ff
	v_cmp_gt_u32_e64 s[0:1], s0, v2
	s_mov_b32 s9, 0
	v_mad_i32_i24 v71, v1, s4, v2
	s_mov_b64 s[6:7], -1
	v_mov_b32_e32 v8, v9
	v_mov_b32_e32 v7, v9
	v_mov_b32_e32 v6, v9
	v_mov_b32_e32 v13, v9
	v_mov_b32_e32 v12, v9
	v_mov_b32_e32 v11, v9
	v_mov_b32_e32 v10, v9
	v_mov_b32_e32 v17, v9
	v_mov_b32_e32 v16, v9
	v_mov_b32_e32 v15, v9
	v_mov_b32_e32 v14, v9
	v_mov_b32_e32 v37, v9
	v_mov_b32_e32 v36, v9
	v_mov_b32_e32 v35, v9
	v_mov_b32_e32 v34, v9
	s_waitcnt lgkmcnt(0)
	s_barrier
	s_and_saveexec_b64 s[4:5], s[0:1]
	s_cbranch_execz .LBB2_34
	s_movk_i32 s0, 0x4b
	v_mov_b32_e32 v3, s3
	v_mov_b32_e32 v4, s15
	v_cmp_gt_u32_e64 s[0:1], s0, v2
	v_mov_b32_e32 v2, s2
	v_mov_b32_e32 v6, 0x100
	v_cndmask_b32_e64 v3, v3, v4, s[0:1]
	v_mov_b32_e32 v4, s14
	v_cndmask_b32_e64 v2, v2, v4, s[0:1]
	v_cmp_lt_u32_e64 s[0:1], s10, v0
	s_mul_i32 s8, s22, 0x25800
	v_lshlrev_b32_e32 v4, 2, v71
	v_cndmask_b32_e64 v11, 0, v6, s[0:1]
	v_mov_b32_e32 v6, 0x12c00
	v_cndmask_b32_e64 v8, 0, v6, s[0:1]
	v_mov_b32_e32 v9, 0
	v_ashrrev_i32_e32 v5, 31, v4
	v_lshl_add_u64 v[6:7], s[8:9], 0, v[8:9]
	v_lshl_add_u64 v[4:5], v[4:5], 2, v[6:7]
	v_lshl_add_u64 v[2:3], v[2:3], 0, v[4:5]
	s_mov_b64 s[2:3], 0x4658
	v_lshlrev_b32_e32 v10, 11, v72
	v_lshl_add_u64 v[62:63], v[2:3], 0, s[2:3]
	s_mov_b32 s2, 0xc000
	v_or3_b32 v73, v10, v11, s2
	s_mov_b32 s8, -16
	s_movk_i32 s9, 0xc000
	s_movk_i32 s10, 0xd000
	s_movk_i32 s11, 0xe000
	s_movk_i32 s14, 0xf000
	s_mov_b64 s[6:7], 0x4b00
	v_mov_b32_e32 v8, v9
	v_mov_b32_e32 v6, v9
	v_mov_b32_e32 v7, v9
	v_mov_b32_e32 v12, v9
	v_mov_b32_e32 v13, v9
	v_mov_b32_e32 v10, v9
	v_mov_b32_e32 v11, v9
	v_mov_b32_e32 v16, v9
	v_mov_b32_e32 v17, v9
	v_mov_b32_e32 v14, v9
	v_mov_b32_e32 v15, v9
	v_mov_b32_e32 v36, v9
	v_mov_b32_e32 v37, v9
	v_mov_b32_e32 v34, v9
	v_mov_b32_e32 v35, v9

	.amdhsa_kernel _Z13attend_kernelPKfS0_S0_S0_S0_S0_S0_S0_S0_S0_PDF16_
		.amdhsa_group_segment_fixed_size 70336
		.amdhsa_private_segment_fixed_size 0
		.amdhsa_kernarg_size 88
		.amdhsa_user_sgpr_count 2
		.amdhsa_user_sgpr_dispatch_ptr 0
		.amdhsa_user_sgpr_queue_ptr 0
		.amdhsa_user_sgpr_kernarg_segment_ptr 1
		.amdhsa_user_sgpr_dispatch_id 0
		.amdhsa_user_sgpr_kernarg_preload_length 0
		.amdhsa_user_sgpr_kernarg_preload_offset 0
		.amdhsa_user_sgpr_private_segment_size 0
		.amdhsa_uses_dynamic_stack 0
		.amdhsa_enable_private_segment 0
		.amdhsa_system_sgpr_workgroup_id_x 1
		.amdhsa_system_sgpr_workgroup_id_y 0
		.amdhsa_system_sgpr_workgroup_id_z 0
		.amdhsa_system_sgpr_workgroup_info 0
		.amdhsa_system_vgpr_workitem_id 0
		.amdhsa_next_free_vgpr 86
		.amdhsa_next_free_sgpr 34
		.amdhsa_accum_offset 88
		.amdhsa_reserve_vcc 1
		.amdhsa_float_round_mode_32 0
		.amdhsa_float_round_mode_16_64 0
		.amdhsa_float_denorm_mode_32 3
		.amdhsa_float_denorm_mode_16_64 3
		.amdhsa_dx10_clamp 1
		.amdhsa_ieee_mode 1
		.amdhsa_fp16_overflow 0
		.amdhsa_tg_split 0
		.amdhsa_exception_fp_ieee_invalid_op 0
		.amdhsa_exception_fp_denorm_src 0
		.amdhsa_exception_fp_ieee_div_zero 0
		.amdhsa_exception_fp_ieee_overflow 0
		.amdhsa_exception_fp_ieee_underflow 0
		.amdhsa_exception_fp_ieee_inexact 0
		.amdhsa_exception_int_div_zero 0
	.end_amdhsa_kernel

.LBB3_36:
	s_or_b64 exec, exec, s[12:13]
	s_waitcnt vmcnt(62) lgkmcnt(2)
	v_fma_f32 v6, v86, v4, 0
	v_fmac_f32_e32 v6, v85, v5
	s_waitcnt vmcnt(61) lgkmcnt(1)
	v_fmac_f32_e32 v6, v84, v2
	s_waitcnt vmcnt(60)
	v_fmac_f32_e32 v6, v83, v3
	v_mbcnt_lo_u32_b32 v83, -1, 0
	v_mbcnt_hi_u32_b32 v83, -1, v83
	v_and_b32_e32 v84, 64, v83
	v_add_u32_e32 v84, 64, v84
	v_xor_b32_e32 v85, 32, v83
	v_cmp_lt_i32_e32 vcc, v85, v84
	s_waitcnt lgkmcnt(0)
	v_fmac_f32_e32 v6, v87, v14
	v_xor_b32_e32 v86, 16, v83
	v_cndmask_b32_e32 v85, v83, v85, vcc
	v_lshlrev_b32_e32 v114, 2, v85
	v_cmp_lt_i32_e32 vcc, v86, v84
	s_load_dword s3, s[4:5], 0x0
	v_cmp_eq_u32_e64 s[4:5], 0, v1
	v_cndmask_b32_e32 v86, v83, v86, vcc
	v_lshlrev_b32_e32 v115, 2, v86
	v_xor_b32_e32 v86, 8, v83
	v_cmp_lt_i32_e32 vcc, v86, v84
	v_cndmask_b32_e32 v86, v83, v86, vcc
	v_lshlrev_b32_e32 v116, 2, v86
	v_xor_b32_e32 v86, 4, v83
	v_cmp_lt_i32_e32 vcc, v86, v84
	v_cndmask_b32_e32 v86, v83, v86, vcc
	v_lshlrev_b32_e32 v117, 2, v86
	v_xor_b32_e32 v86, 2, v83
	v_cmp_lt_i32_e32 vcc, v86, v84
	v_cndmask_b32_e32 v86, v83, v86, vcc
	v_lshlrev_b32_e32 v118, 2, v86
	v_xor_b32_e32 v86, 1, v83
	v_cmp_lt_i32_e32 vcc, v86, v84
	s_nop 1
	v_cndmask_b32_e32 v83, v83, v86, vcc
	v_lshlrev_b32_e32 v119, 2, v83
	s_waitcnt lgkmcnt(0)
	s_nop 1
	v_add_f32_dpp v83, v6, v6 quad_perm:[1,0,3,2] row_mask:0xf bank_mask:0xf
	s_nop 1
	v_add_f32_dpp v83, v83, v83 quad_perm:[2,3,0,1] row_mask:0xf bank_mask:0xf
	s_nop 1
	v_add_f32_dpp v83, v83, v83 row_half_mirror row_mask:0xf bank_mask:0xf
	s_nop 1
	v_add_f32_dpp v83, v83, v83 row_mirror row_mask:0xf bank_mask:0xf
	s_nop 1
	v_readlane_b32 s20, v83, 0
	v_readlane_b32 s21, v83, 16
	v_readlane_b32 s22, v83, 32
	v_readlane_b32 s23, v83, 48
	v_mov_b32_e32 v83, s20
	v_add_f32_e32 v83, s21, v83
	v_add_f32_e32 v83, s22, v83
	v_add_f32_e32 v83, s23, v83
	v_and_b32_e32 v6, 0x1c0, v0
	s_and_saveexec_b64 s[12:13], s[4:5]
	s_cbranch_execz .LBB3_38
	s_waitcnt lgkmcnt(0)
	v_add_f32_e32 v83, s3, v83
	ds_write_b32 v6, v83 offset:8576
.LBB3_38:
	s_or_b64 exec, exec, s[12:13]
	s_waitcnt vmcnt(59)
	v_fma_f32 v82, v82, v4, 0
	s_waitcnt vmcnt(58)
	v_fmac_f32_e32 v82, v81, v5
	s_waitcnt vmcnt(57)
	v_fmac_f32_e32 v82, v80, v2
	s_waitcnt vmcnt(56)
	v_fmac_f32_e32 v82, v79, v3
	v_fmac_f32_e32 v82, v21, v14
	s_nop 1
	v_add_f32_dpp v21, v82, v82 quad_perm:[1,0,3,2] row_mask:0xf bank_mask:0xf
	s_nop 1
	v_add_f32_dpp v21, v21, v21 quad_perm:[2,3,0,1] row_mask:0xf bank_mask:0xf
	s_nop 1
	v_add_f32_dpp v21, v21, v21 row_half_mirror row_mask:0xf bank_mask:0xf
	s_nop 1
	v_add_f32_dpp v21, v21, v21 row_mirror row_mask:0xf bank_mask:0xf
	s_nop 1
	v_readlane_b32 s20, v21, 0
	v_readlane_b32 s21, v21, 16
	v_readlane_b32 s22, v21, 32
	v_readlane_b32 s23, v21, 48
	v_mov_b32_e32 v21, s20
	v_add_f32_e32 v21, s21, v21
	v_add_f32_e32 v21, s22, v21
	v_add_f32_e32 v21, s23, v21
	s_and_saveexec_b64 s[12:13], s[4:5]
	s_cbranch_execz .LBB3_40
	s_waitcnt lgkmcnt(0)
	v_add_f32_e32 v21, s3, v21
	ds_write_b32 v6, v21 offset:8580
.LBB3_40:
	s_or_b64 exec, exec, s[12:13]
	s_waitcnt vmcnt(55)
	v_fma_f32 v21, v76, v4, 0
	s_waitcnt vmcnt(54)
	v_fmac_f32_e32 v21, v77, v5
	s_waitcnt vmcnt(53)
	v_fmac_f32_e32 v21, v75, v2
	s_waitcnt vmcnt(52)
	v_fmac_f32_e32 v21, v74, v3
	v_fmac_f32_e32 v21, v78, v14
	s_nop 1
	v_add_f32_dpp v21, v21, v21 quad_perm:[1,0,3,2] row_mask:0xf bank_mask:0xf
	s_nop 1
	v_add_f32_dpp v21, v21, v21 quad_perm:[2,3,0,1] row_mask:0xf bank_mask:0xf
	s_nop 1
	v_add_f32_dpp v21, v21, v21 row_half_mirror row_mask:0xf bank_mask:0xf
	s_nop 1
	v_add_f32_dpp v21, v21, v21 row_mirror row_mask:0xf bank_mask:0xf
	s_nop 1
	v_readlane_b32 s20, v21, 0
	v_readlane_b32 s21, v21, 16
	v_readlane_b32 s22, v21, 32
	v_readlane_b32 s23, v21, 48
	v_mov_b32_e32 v21, s20
	v_add_f32_e32 v21, s21, v21
	v_add_f32_e32 v21, s22, v21
	v_add_f32_e32 v21, s23, v21
	s_and_saveexec_b64 s[12:13], s[4:5]
	s_cbranch_execz .LBB3_42
	s_waitcnt lgkmcnt(0)
	v_add_f32_e32 v21, s3, v21
	ds_write_b32 v6, v21 offset:8584
.LBB3_42:
	s_or_b64 exec, exec, s[12:13]
	s_waitcnt vmcnt(51)
	v_fma_f32 v21, v73, v4, 0
	s_waitcnt vmcnt(50)
	v_fmac_f32_e32 v21, v72, v5
	s_waitcnt vmcnt(49)
	v_fmac_f32_e32 v21, v71, v2
	s_waitcnt vmcnt(48)
	v_fmac_f32_e32 v21, v70, v3
	v_fmac_f32_e32 v21, v19, v14
	s_nop 1
	v_add_f32_dpp v19, v21, v21 quad_perm:[1,0,3,2] row_mask:0xf bank_mask:0xf
	s_nop 1
	v_add_f32_dpp v19, v19, v19 quad_perm:[2,3,0,1] row_mask:0xf bank_mask:0xf
	s_nop 1
	v_add_f32_dpp v19, v19, v19 row_half_mirror row_mask:0xf bank_mask:0xf
	s_nop 1
	v_add_f32_dpp v19, v19, v19 row_mirror row_mask:0xf bank_mask:0xf
	s_nop 1
	v_readlane_b32 s20, v19, 0
	v_readlane_b32 s21, v19, 16
	v_readlane_b32 s22, v19, 32
	v_readlane_b32 s23, v19, 48
	v_mov_b32_e32 v19, s20
	v_add_f32_e32 v19, s21, v19
	v_add_f32_e32 v19, s22, v19
	v_add_f32_e32 v19, s23, v19
	s_and_saveexec_b64 s[12:13], s[4:5]
	s_cbranch_execz .LBB3_44
	s_waitcnt lgkmcnt(0)
	v_add_f32_e32 v19, s3, v19
	ds_write_b32 v6, v19 offset:8588
.LBB3_44:
	s_or_b64 exec, exec, s[12:13]
	s_waitcnt vmcnt(47)
	v_fma_f32 v19, v68, v4, 0
	s_waitcnt vmcnt(46)
	v_fmac_f32_e32 v19, v67, v5
	s_waitcnt vmcnt(45)
	v_fmac_f32_e32 v19, v66, v2
	s_waitcnt vmcnt(44)
	v_fmac_f32_e32 v19, v65, v3
	v_fmac_f32_e32 v19, v69, v14
	s_waitcnt lgkmcnt(0)
	s_nop 1
	v_add_f32_dpp v19, v19, v19 quad_perm:[1,0,3,2] row_mask:0xf bank_mask:0xf
	s_nop 1
	v_add_f32_dpp v19, v19, v19 quad_perm:[2,3,0,1] row_mask:0xf bank_mask:0xf
	s_nop 1
	v_add_f32_dpp v19, v19, v19 row_half_mirror row_mask:0xf bank_mask:0xf
	s_nop 1
	v_add_f32_dpp v19, v19, v19 row_mirror row_mask:0xf bank_mask:0xf
	s_nop 1
	v_readlane_b32 s20, v19, 0
	v_readlane_b32 s21, v19, 16
	v_readlane_b32 s22, v19, 32
	v_readlane_b32 s23, v19, 48
	v_mov_b32_e32 v19, s20
	v_add_f32_e32 v19, s21, v19
	v_add_f32_e32 v19, s22, v19
	v_add_f32_e32 v19, s23, v19
	s_and_saveexec_b64 s[12:13], s[4:5]
	s_cbranch_execz .LBB3_46
	s_waitcnt lgkmcnt(0)
	v_add_f32_e32 v19, s3, v19
	ds_write_b32 v6, v19 offset:8592
.LBB3_46:
	s_or_b64 exec, exec, s[12:13]
	s_waitcnt vmcnt(43)
	v_fma_f32 v19, v64, v4, 0
	s_waitcnt vmcnt(42)
	v_fmac_f32_e32 v19, v63, v5
	s_waitcnt vmcnt(41)
	v_fmac_f32_e32 v19, v62, v2
	s_waitcnt vmcnt(40)
	v_fmac_f32_e32 v19, v61, v3
	v_fmac_f32_e32 v19, v17, v14
	s_nop 1
	v_add_f32_dpp v17, v19, v19 quad_perm:[1,0,3,2] row_mask:0xf bank_mask:0xf
	s_nop 1
	v_add_f32_dpp v17, v17, v17 quad_perm:[2,3,0,1] row_mask:0xf bank_mask:0xf
	s_nop 1
	v_add_f32_dpp v17, v17, v17 row_half_mirror row_mask:0xf bank_mask:0xf
	s_nop 1
	v_add_f32_dpp v17, v17, v17 row_mirror row_mask:0xf bank_mask:0xf
	s_nop 1
	v_readlane_b32 s20, v17, 0
	v_readlane_b32 s21, v17, 16
	v_readlane_b32 s22, v17, 32
	v_readlane_b32 s23, v17, 48
	v_mov_b32_e32 v17, s20
	v_add_f32_e32 v17, s21, v17
	v_add_f32_e32 v17, s22, v17
	v_add_f32_e32 v17, s23, v17
	s_and_saveexec_b64 s[12:13], s[4:5]
	s_cbranch_execz .LBB3_48
	s_waitcnt lgkmcnt(0)
	v_add_f32_e32 v17, s3, v17
	ds_write_b32 v6, v17 offset:8596
.LBB3_48:
	s_or_b64 exec, exec, s[12:13]
	s_waitcnt vmcnt(39)
	v_fma_f32 v17, v59, v4, 0
	s_waitcnt vmcnt(38)
	v_fmac_f32_e32 v17, v58, v5
	s_waitcnt vmcnt(37)
	v_fmac_f32_e32 v17, v57, v2
	s_waitcnt vmcnt(36)
	v_fmac_f32_e32 v17, v56, v3
	v_fmac_f32_e32 v17, v60, v14
	s_waitcnt lgkmcnt(0)
	s_nop 1
	v_add_f32_dpp v17, v17, v17 quad_perm:[1,0,3,2] row_mask:0xf bank_mask:0xf
	s_nop 1
	v_add_f32_dpp v17, v17, v17 quad_perm:[2,3,0,1] row_mask:0xf bank_mask:0xf
	s_nop 1
	v_add_f32_dpp v17, v17, v17 row_half_mirror row_mask:0xf bank_mask:0xf
	s_nop 1
	v_add_f32_dpp v17, v17, v17 row_mirror row_mask:0xf bank_mask:0xf
	s_nop 1
	v_readlane_b32 s20, v17, 0
	v_readlane_b32 s21, v17, 16
	v_readlane_b32 s22, v17, 32
	v_readlane_b32 s23, v17, 48
	v_mov_b32_e32 v17, s20
	v_add_f32_e32 v17, s21, v17
	v_add_f32_e32 v17, s22, v17
	v_add_f32_e32 v17, s23, v17
	s_and_saveexec_b64 s[12:13], s[4:5]
	s_cbranch_execz .LBB3_50
	s_waitcnt lgkmcnt(0)
	v_add_f32_e32 v17, s3, v17
	ds_write_b32 v6, v17 offset:8600
.LBB3_50:
	s_or_b64 exec, exec, s[12:13]
	s_waitcnt vmcnt(35)
	v_fma_f32 v17, v54, v4, 0
	s_waitcnt vmcnt(34)
	v_fmac_f32_e32 v17, v52, v5
	s_waitcnt vmcnt(33)
	v_fmac_f32_e32 v17, v50, v2
	s_waitcnt vmcnt(32)
	v_fmac_f32_e32 v17, v48, v3
	v_fmac_f32_e32 v17, v15, v14
	s_nop 1
	v_add_f32_dpp v15, v17, v17 quad_perm:[1,0,3,2] row_mask:0xf bank_mask:0xf
	s_nop 1
	v_add_f32_dpp v15, v15, v15 quad_perm:[2,3,0,1] row_mask:0xf bank_mask:0xf
	s_nop 1
	v_add_f32_dpp v15, v15, v15 row_half_mirror row_mask:0xf bank_mask:0xf
	s_nop 1
	v_add_f32_dpp v15, v15, v15 row_mirror row_mask:0xf bank_mask:0xf
	s_nop 1
	v_readlane_b32 s20, v15, 0
	v_readlane_b32 s21, v15, 16
	v_readlane_b32 s22, v15, 32
	v_readlane_b32 s23, v15, 48
	v_mov_b32_e32 v15, s20
	v_add_f32_e32 v15, s21, v15
	v_add_f32_e32 v15, s22, v15
	v_add_f32_e32 v15, s23, v15
	s_and_saveexec_b64 s[12:13], s[4:5]
	s_cbranch_execz .LBB3_52
	s_waitcnt lgkmcnt(0)
	v_add_f32_e32 v15, s3, v15
	ds_write_b32 v6, v15 offset:8604
.LBB3_52:
	s_or_b64 exec, exec, s[12:13]
	s_waitcnt vmcnt(31)
	v_fma_f32 v15, v53, v4, 0
	s_waitcnt vmcnt(30)
	v_fmac_f32_e32 v15, v51, v5
	s_waitcnt vmcnt(29)
	v_fmac_f32_e32 v15, v49, v2
	s_waitcnt vmcnt(28)
	v_fmac_f32_e32 v15, v47, v3
	v_fmac_f32_e32 v15, v55, v14
	s_waitcnt lgkmcnt(0)
	s_nop 1
	v_add_f32_dpp v15, v15, v15 quad_perm:[1,0,3,2] row_mask:0xf bank_mask:0xf
	s_nop 1
	v_add_f32_dpp v15, v15, v15 quad_perm:[2,3,0,1] row_mask:0xf bank_mask:0xf
	s_nop 1
	v_add_f32_dpp v15, v15, v15 row_half_mirror row_mask:0xf bank_mask:0xf
	s_nop 1
	v_add_f32_dpp v15, v15, v15 row_mirror row_mask:0xf bank_mask:0xf
	s_nop 1
	v_readlane_b32 s20, v15, 0
	v_readlane_b32 s21, v15, 16
	v_readlane_b32 s22, v15, 32
	v_readlane_b32 s23, v15, 48
	v_mov_b32_e32 v15, s20
	v_add_f32_e32 v15, s21, v15
	v_add_f32_e32 v15, s22, v15
	v_add_f32_e32 v15, s23, v15
	s_and_saveexec_b64 s[12:13], s[4:5]
	s_cbranch_execz .LBB3_54
	s_waitcnt lgkmcnt(0)
	v_add_f32_e32 v15, s3, v15
	ds_write_b32 v6, v15 offset:8608
.LBB3_54:
	s_or_b64 exec, exec, s[12:13]
	s_waitcnt vmcnt(27)
	v_fma_f32 v15, v46, v4, 0
	s_waitcnt vmcnt(26)
	v_fmac_f32_e32 v15, v45, v5
	s_waitcnt vmcnt(25)
	v_fmac_f32_e32 v15, v44, v2
	s_waitcnt vmcnt(24)
	v_fmac_f32_e32 v15, v43, v3
	v_fmac_f32_e32 v15, v13, v14
	s_nop 1
	v_add_f32_dpp v13, v15, v15 quad_perm:[1,0,3,2] row_mask:0xf bank_mask:0xf
	s_nop 1
	v_add_f32_dpp v13, v13, v13 quad_perm:[2,3,0,1] row_mask:0xf bank_mask:0xf
	s_nop 1
	v_add_f32_dpp v13, v13, v13 row_half_mirror row_mask:0xf bank_mask:0xf
	s_nop 1
	v_add_f32_dpp v13, v13, v13 row_mirror row_mask:0xf bank_mask:0xf
	s_nop 1
	v_readlane_b32 s20, v13, 0
	v_readlane_b32 s21, v13, 16
	v_readlane_b32 s22, v13, 32
	v_readlane_b32 s23, v13, 48
	v_mov_b32_e32 v13, s20
	v_add_f32_e32 v13, s21, v13
	v_add_f32_e32 v13, s22, v13
	v_add_f32_e32 v13, s23, v13
	s_and_saveexec_b64 s[12:13], s[4:5]
	s_cbranch_execz .LBB3_56
	s_waitcnt lgkmcnt(0)
	v_add_f32_e32 v13, s3, v13
	ds_write_b32 v6, v13 offset:8612
.LBB3_56:
	s_or_b64 exec, exec, s[12:13]
	s_waitcnt vmcnt(23)
	v_fma_f32 v13, v41, v4, 0
	s_waitcnt vmcnt(22)
	v_fmac_f32_e32 v13, v40, v5
	s_waitcnt vmcnt(21)
	v_fmac_f32_e32 v13, v39, v2
	s_waitcnt vmcnt(20)
	v_fmac_f32_e32 v13, v38, v3
	v_fmac_f32_e32 v13, v42, v14
	s_waitcnt lgkmcnt(0)
	s_nop 1
	v_add_f32_dpp v13, v13, v13 quad_perm:[1,0,3,2] row_mask:0xf bank_mask:0xf
	s_nop 1
	v_add_f32_dpp v13, v13, v13 quad_perm:[2,3,0,1] row_mask:0xf bank_mask:0xf
	s_nop 1
	v_add_f32_dpp v13, v13, v13 row_half_mirror row_mask:0xf bank_mask:0xf
	s_nop 1
	v_add_f32_dpp v13, v13, v13 row_mirror row_mask:0xf bank_mask:0xf
	s_nop 1
	v_readlane_b32 s20, v13, 0
	v_readlane_b32 s21, v13, 16
	v_readlane_b32 s22, v13, 32
	v_readlane_b32 s23, v13, 48
	v_mov_b32_e32 v13, s20
	v_add_f32_e32 v13, s21, v13
	v_add_f32_e32 v13, s22, v13
	v_add_f32_e32 v13, s23, v13
	s_and_saveexec_b64 s[12:13], s[4:5]
	s_cbranch_execz .LBB3_58
	s_waitcnt lgkmcnt(0)
	v_add_f32_e32 v13, s3, v13
	ds_write_b32 v6, v13 offset:8616
.LBB3_58:
	s_or_b64 exec, exec, s[12:13]
	s_waitcnt vmcnt(19)
	v_fma_f32 v13, v37, v4, 0
	s_waitcnt vmcnt(18)
	v_fmac_f32_e32 v13, v36, v5
	s_waitcnt vmcnt(17)
	v_fmac_f32_e32 v13, v35, v2
	s_waitcnt vmcnt(16)
	v_fmac_f32_e32 v13, v34, v3
	v_fmac_f32_e32 v13, v11, v14
	s_nop 1
	v_add_f32_dpp v11, v13, v13 quad_perm:[1,0,3,2] row_mask:0xf bank_mask:0xf
	s_nop 1
	v_add_f32_dpp v11, v11, v11 quad_perm:[2,3,0,1] row_mask:0xf bank_mask:0xf
	s_nop 1
	v_add_f32_dpp v11, v11, v11 row_half_mirror row_mask:0xf bank_mask:0xf
	s_nop 1
	v_add_f32_dpp v11, v11, v11 row_mirror row_mask:0xf bank_mask:0xf
	s_nop 1
	v_readlane_b32 s20, v11, 0
	v_readlane_b32 s21, v11, 16
	v_readlane_b32 s22, v11, 32
	v_readlane_b32 s23, v11, 48
	v_mov_b32_e32 v11, s20
	v_add_f32_e32 v11, s21, v11
	v_add_f32_e32 v11, s22, v11
	v_add_f32_e32 v11, s23, v11
	s_and_saveexec_b64 s[12:13], s[4:5]
	s_cbranch_execz .LBB3_60
	s_waitcnt lgkmcnt(0)
	v_add_f32_e32 v11, s3, v11
	ds_write_b32 v6, v11 offset:8620
.LBB3_60:
	s_or_b64 exec, exec, s[12:13]
	s_waitcnt vmcnt(15)
	v_fma_f32 v11, v32, v4, 0
	s_waitcnt vmcnt(14)
	v_fmac_f32_e32 v11, v31, v5
	s_waitcnt vmcnt(13)
	v_fmac_f32_e32 v11, v30, v2
	s_waitcnt vmcnt(12)
	v_fmac_f32_e32 v11, v29, v3
	v_fmac_f32_e32 v11, v33, v14
	s_waitcnt lgkmcnt(0)
	s_nop 1
	v_add_f32_dpp v11, v11, v11 quad_perm:[1,0,3,2] row_mask:0xf bank_mask:0xf
	s_nop 1
	v_add_f32_dpp v11, v11, v11 quad_perm:[2,3,0,1] row_mask:0xf bank_mask:0xf
	s_nop 1
	v_add_f32_dpp v11, v11, v11 row_half_mirror row_mask:0xf bank_mask:0xf
	s_nop 1
	v_add_f32_dpp v11, v11, v11 row_mirror row_mask:0xf bank_mask:0xf
	s_nop 1
	v_readlane_b32 s20, v11, 0
	v_readlane_b32 s21, v11, 16
	v_readlane_b32 s22, v11, 32
	v_readlane_b32 s23, v11, 48
	v_mov_b32_e32 v11, s20
	v_add_f32_e32 v11, s21, v11
	v_add_f32_e32 v11, s22, v11
	v_add_f32_e32 v11, s23, v11
	s_and_saveexec_b64 s[12:13], s[4:5]
	s_cbranch_execz .LBB3_62
	s_waitcnt lgkmcnt(0)
	v_add_f32_e32 v11, s3, v11
	ds_write_b32 v6, v11 offset:8624
.LBB3_62:
	s_or_b64 exec, exec, s[12:13]
	s_waitcnt vmcnt(11)
	v_fma_f32 v11, v28, v4, 0
	s_waitcnt vmcnt(10)
	v_fmac_f32_e32 v11, v27, v5
	s_waitcnt vmcnt(9)
	v_fmac_f32_e32 v11, v26, v2
	s_waitcnt vmcnt(8)
	v_fmac_f32_e32 v11, v25, v3
	v_fmac_f32_e32 v11, v9, v14
	s_nop 1
	v_add_f32_dpp v9, v11, v11 quad_perm:[1,0,3,2] row_mask:0xf bank_mask:0xf
	s_nop 1
	v_add_f32_dpp v9, v9, v9 quad_perm:[2,3,0,1] row_mask:0xf bank_mask:0xf
	s_nop 1
	v_add_f32_dpp v9, v9, v9 row_half_mirror row_mask:0xf bank_mask:0xf
	s_nop 1
	v_add_f32_dpp v9, v9, v9 row_mirror row_mask:0xf bank_mask:0xf
	s_nop 1
	v_readlane_b32 s20, v9, 0
	v_readlane_b32 s21, v9, 16
	v_readlane_b32 s22, v9, 32
	v_readlane_b32 s23, v9, 48
	v_mov_b32_e32 v9, s20
	v_add_f32_e32 v9, s21, v9
	v_add_f32_e32 v9, s22, v9
	v_add_f32_e32 v9, s23, v9
	s_and_saveexec_b64 s[12:13], s[4:5]
	s_cbranch_execz .LBB3_64
	s_waitcnt lgkmcnt(0)
	v_add_f32_e32 v9, s3, v9
	ds_write_b32 v6, v9 offset:8628
.LBB3_64:
	s_or_b64 exec, exec, s[12:13]
	s_waitcnt vmcnt(7)
	v_fma_f32 v9, v23, v4, 0
	s_waitcnt vmcnt(6)
	v_fmac_f32_e32 v9, v22, v5
	s_waitcnt vmcnt(5)
	v_fmac_f32_e32 v9, v20, v2
	s_waitcnt vmcnt(4)
	v_fmac_f32_e32 v9, v18, v3
	v_fmac_f32_e32 v9, v24, v14
	s_waitcnt lgkmcnt(0)
	s_nop 1
	v_add_f32_dpp v9, v9, v9 quad_perm:[1,0,3,2] row_mask:0xf bank_mask:0xf
	s_nop 1
	v_add_f32_dpp v9, v9, v9 quad_perm:[2,3,0,1] row_mask:0xf bank_mask:0xf
	s_nop 1
	v_add_f32_dpp v9, v9, v9 row_half_mirror row_mask:0xf bank_mask:0xf
	s_nop 1
	v_add_f32_dpp v9, v9, v9 row_mirror row_mask:0xf bank_mask:0xf
	s_nop 1
	v_readlane_b32 s20, v9, 0
	v_readlane_b32 s21, v9, 16
	v_readlane_b32 s22, v9, 32
	v_readlane_b32 s23, v9, 48
	v_mov_b32_e32 v9, s20
	v_add_f32_e32 v9, s21, v9
	v_add_f32_e32 v9, s22, v9
	v_add_f32_e32 v9, s23, v9
	s_and_saveexec_b64 s[12:13], s[4:5]
	s_cbranch_execz .LBB3_66
	s_waitcnt lgkmcnt(0)
	v_add_f32_e32 v9, s3, v9
	ds_write_b32 v6, v9 offset:8632
.LBB3_66:
	s_or_b64 exec, exec, s[12:13]
	s_waitcnt vmcnt(3)
	v_fma_f32 v4, v16, v4, 0
	s_waitcnt vmcnt(2)
	v_fmac_f32_e32 v4, v12, v5
	s_waitcnt vmcnt(1)
	v_fmac_f32_e32 v4, v10, v2
	s_waitcnt vmcnt(0)
	v_fmac_f32_e32 v4, v8, v3
	v_fmac_f32_e32 v4, v7, v14
	s_nop 1
	v_add_f32_dpp v2, v4, v4 quad_perm:[1,0,3,2] row_mask:0xf bank_mask:0xf
	s_nop 1
	v_add_f32_dpp v2, v2, v2 quad_perm:[2,3,0,1] row_mask:0xf bank_mask:0xf
	s_nop 1
	v_add_f32_dpp v2, v2, v2 row_half_mirror row_mask:0xf bank_mask:0xf
	s_nop 1
	v_add_f32_dpp v2, v2, v2 row_mirror row_mask:0xf bank_mask:0xf
	s_nop 1
	v_readlane_b32 s20, v2, 0
	v_readlane_b32 s21, v2, 16
	v_readlane_b32 s22, v2, 32
	v_readlane_b32 s23, v2, 48
	v_mov_b32_e32 v2, s20
	v_add_f32_e32 v2, s21, v2
	v_add_f32_e32 v2, s22, v2
	v_add_f32_e32 v2, s23, v2
	s_and_saveexec_b64 s[12:13], s[4:5]
	s_cbranch_execz .LBB3_68
	s_waitcnt lgkmcnt(0)
	v_add_f32_e32 v2, s3, v2
	ds_write_b32 v6, v2 offset:8636
.LBB3_68:
	s_or_b64 exec, exec, s[12:13]
	v_cmp_gt_u32_e32 vcc, 64, v0
	v_lshlrev_b32_e32 v120, 2, v0
	s_waitcnt lgkmcnt(0)
	s_barrier
	s_and_saveexec_b64 s[12:13], vcc
	s_cbranch_execz .LBB3_70
	ds_read_b32 v2, v120 offset:8832
	ds_read_b32 v3, v91 offset:8576
	s_waitcnt lgkmcnt(1)
	v_max_f32_e32 v4, v2, v2
	s_waitcnt lgkmcnt(0)
	v_max_f32_e32 v5, v3, v3
	v_max_f32_e32 v4, v5, v4
	s_nop 1
	v_max_f32_dpp v4, v4, v4 quad_perm:[1,0,3,2] row_mask:0xf bank_mask:0xf
	s_nop 1
	v_max_f32_dpp v4, v4, v4 quad_perm:[2,3,0,1] row_mask:0xf bank_mask:0xf
	s_nop 1
	v_max_f32_dpp v4, v4, v4 row_half_mirror row_mask:0xf bank_mask:0xf
	s_nop 1
	v_max_f32_dpp v4, v4, v4 row_mirror row_mask:0xf bank_mask:0xf
	s_nop 1
	v_readlane_b32 s20, v4, 0
	v_readlane_b32 s21, v4, 16
	v_readlane_b32 s22, v4, 32
	v_readlane_b32 s23, v4, 48
	v_mov_b32_e32 v4, s20
	v_max_f32_e32 v4, s21, v4
	v_max_f32_e32 v4, s22, v4
	v_max_f32_e32 v4, s23, v4
	v_sub_f32_e32 v3, v3, v4
	v_sub_f32_e32 v2, v2, v4
	v_mul_f32_e32 v3, 0x3fb8aa3b, v3
	v_mul_f32_e32 v2, 0x3fb8aa3b, v2
	v_exp_f32_e32 v3, v3
	v_exp_f32_e32 v2, v2
	s_nop 0
	v_add_f32_e32 v4, v3, v2
	s_nop 1
	v_add_f32_dpp v4, v4, v4 quad_perm:[1,0,3,2] row_mask:0xf bank_mask:0xf
	s_nop 1
	v_add_f32_dpp v4, v4, v4 quad_perm:[2,3,0,1] row_mask:0xf bank_mask:0xf
	s_nop 1
	v_add_f32_dpp v4, v4, v4 row_half_mirror row_mask:0xf bank_mask:0xf
	s_nop 1
	v_add_f32_dpp v4, v4, v4 row_mirror row_mask:0xf bank_mask:0xf
	s_nop 1
	v_readlane_b32 s20, v4, 0
	v_readlane_b32 s21, v4, 16
	v_readlane_b32 s22, v4, 32
	v_readlane_b32 s23, v4, 48
	v_mov_b32_e32 v4, s20
	v_add_f32_e32 v4, s21, v4
	v_add_f32_e32 v4, s22, v4
	v_add_f32_e32 v4, s23, v4
	s_waitcnt lgkmcnt(0)
	v_div_scale_f32 v5, s[14:15], v4, v4, 1.0
	v_rcp_f32_e32 v6, v5
	v_div_scale_f32 v7, vcc, 1.0, v4, 1.0
	v_fma_f32 v8, -v5, v6, 1.0
	v_fmac_f32_e32 v6, v8, v6
	v_mul_f32_e32 v8, v7, v6
	v_fma_f32 v9, -v5, v8, v7
	v_fmac_f32_e32 v8, v9, v6
	v_fma_f32 v5, -v5, v8, v7
	v_div_fmas_f32 v5, v5, v6, v8
	v_div_fixup_f32 v4, v5, v4, 1.0
	v_mul_f32_e32 v3, v3, v4
	v_mul_f32_e32 v2, v2, v4
	ds_write_b32 v91, v3 offset:8576
	ds_write_b32 v120, v2 offset:8832

.LBB3_81:
	s_or_b64 exec, exec, s[10:11]
	s_nop 1
	v_add_f32_dpp v0, v2, v2 quad_perm:[1,0,3,2] row_mask:0xf bank_mask:0xf
	s_nop 1
	v_add_f32_dpp v0, v0, v0 quad_perm:[2,3,0,1] row_mask:0xf bank_mask:0xf
	s_nop 1
	v_add_f32_dpp v0, v0, v0 row_half_mirror row_mask:0xf bank_mask:0xf
	s_nop 1
	v_add_f32_dpp v0, v0, v0 row_mirror row_mask:0xf bank_mask:0xf
	s_nop 1
	v_readlane_b32 s20, v0, 0
	v_readlane_b32 s21, v0, 16
	v_readlane_b32 s22, v0, 32
	v_readlane_b32 s23, v0, 48
	v_mov_b32_e32 v0, s20
	v_add_f32_e32 v0, s21, v0
	v_add_f32_e32 v0, s22, v0
	v_add_f32_e32 v0, s23, v0
	s_and_b64 exec, exec, s[4:5]
	s_cbranch_execz .LBB3_83
	s_waitcnt lgkmcnt(0)
	v_mul_f32_e32 v1, 0x3c23d70a, v0
	v_cmp_lt_f32_e32 vcc, 0, v0
	s_nop 1
	v_cndmask_b32_e32 v2, v1, v0, vcc
	v_mad_u64_u32 v[0:1], s[0:1], s2, 3, v[90:91]
	v_ashrrev_i32_e32 v1, 31, v0
	v_lshl_add_u64 v[0:1], v[0:1], 2, s[8:9]
	global_store_dword v[0:1], v2, off

	.amdhsa_kernel _Z16postfinal_kernelPKfS0_S0_S0_Pf
		.amdhsa_group_segment_fixed_size 9088
		.amdhsa_private_segment_fixed_size 0
		.amdhsa_kernarg_size 40
		.amdhsa_user_sgpr_count 2
		.amdhsa_user_sgpr_dispatch_ptr 0
		.amdhsa_user_sgpr_queue_ptr 0
		.amdhsa_user_sgpr_kernarg_segment_ptr 1
		.amdhsa_user_sgpr_dispatch_id 0
		.amdhsa_user_sgpr_kernarg_preload_length 0
		.amdhsa_user_sgpr_kernarg_preload_offset 0
		.amdhsa_user_sgpr_private_segment_size 0
		.amdhsa_uses_dynamic_stack 0
		.amdhsa_enable_private_segment 0
		.amdhsa_system_sgpr_workgroup_id_x 1
		.amdhsa_system_sgpr_workgroup_id_y 0
		.amdhsa_system_sgpr_workgroup_id_z 0
		.amdhsa_system_sgpr_workgroup_info 0
		.amdhsa_system_vgpr_workitem_id 0
		.amdhsa_next_free_vgpr 124
		.amdhsa_next_free_sgpr 24
		.amdhsa_accum_offset 124
		.amdhsa_reserve_vcc 1
		.amdhsa_float_round_mode_32 0
		.amdhsa_float_round_mode_16_64 0
		.amdhsa_float_denorm_mode_32 3
		.amdhsa_float_denorm_mode_16_64 3
		.amdhsa_dx10_clamp 1
		.amdhsa_ieee_mode 1
		.amdhsa_fp16_overflow 0
		.amdhsa_tg_split 0
		.amdhsa_exception_fp_ieee_invalid_op 0
		.amdhsa_exception_fp_denorm_src 0
		.amdhsa_exception_fp_ieee_div_zero 0
		.amdhsa_exception_fp_ieee_overflow 0
		.amdhsa_exception_fp_ieee_underflow 0
		.amdhsa_exception_fp_ieee_inexact 0
		.amdhsa_exception_int_div_zero 0
	.end_amdhsa_kernel

amdhsa.kernels:
  - .agpr_count:     16
    .args:
      - .actual_access:  read_only
        .address_space:  global
        .offset:         0
        .size:           8
        .value_kind:     global_buffer
      - .actual_access:  read_only
        .address_space:  global
        .offset:         8
        .size:           8
        .value_kind:     global_buffer
      - .actual_access:  read_only
        .address_space:  global
        .offset:         16
        .size:           8
        .value_kind:     global_buffer
      - .actual_access:  read_only
        .address_space:  global
        .offset:         24
        .size:           8
        .value_kind:     global_buffer
      - .actual_access:  write_only
        .address_space:  global
        .offset:         32
        .size:           8
        .value_kind:     global_buffer
      - .offset:         40
        .size:           4
        .value_kind:     by_value
      - .offset:         44
        .size:           4
        .value_kind:     by_value
      - .offset:         48
        .size:           4
        .value_kind:     by_value
      - .offset:         52
        .size:           4
        .value_kind:     by_value
      - .offset:         56
        .size:           4
        .value_kind:     by_value
      - .offset:         60
        .size:           4
        .value_kind:     by_value
      - .offset:         64
        .size:           4
        .value_kind:     by_value
    .group_segment_fixed_size: 43008
    .kernarg_segment_align: 8
    .kernarg_segment_size: 68
    .language:       OpenCL C
    .language_version:
      - 2
      - 0
    .max_flat_workgroup_size: 256
    .name:           _Z15gemm_f16_kernelPKDF16_S0_PKfS2_Pfiiiiiii
    .private_segment_fixed_size: 0
    .sgpr_count:     33
    .sgpr_spill_count: 0
    .symbol:         _Z15gemm_f16_kernelPKDF16_S0_PKfS2_Pfiiiiiii.kd
    .uniform_work_group_size: 1
    .uses_dynamic_stack: false
    .vgpr_count:     104
    .vgpr_spill_count: 0
    .wavefront_size: 64
  - .agpr_count:     0
    .args:
      - .actual_access:  read_only
        .address_space:  global
        .offset:         0
        .size:           8
        .value_kind:     global_buffer
      - .actual_access:  read_only
        .address_space:  global
        .offset:         8
        .size:           8
        .value_kind:     global_buffer
      - .actual_access:  read_only
        .address_space:  global
        .offset:         16
        .size:           8
        .value_kind:     global_buffer
      - .actual_access:  read_only
        .address_space:  global
        .offset:         24
        .size:           8
        .value_kind:     global_buffer
      - .actual_access:  read_only
        .address_space:  global
        .offset:         32
        .size:           8
        .value_kind:     global_buffer
      - .actual_access:  read_only
        .address_space:  global
        .offset:         40
        .size:           8
        .value_kind:     global_buffer
      - .actual_access:  write_only
        .address_space:  global
        .offset:         48
        .size:           8
        .value_kind:     global_buffer
      - .actual_access:  read_only
        .address_space:  global
        .offset:         56
        .size:           8
        .value_kind:     global_buffer
    .group_segment_fixed_size: 121472
    .kernarg_segment_align: 8
    .kernarg_segment_size: 64
    .language:       OpenCL C
    .language_version:
      - 2
      - 0
    .max_flat_workgroup_size: 512
    .name:           _Z15score_ds_kernelPKfS0_S0_S0_S0_S0_PfPKDF16_
    .private_segment_fixed_size: 0
    .sgpr_count:     32
    .sgpr_spill_count: 0
    .symbol:         _Z15score_ds_kernelPKfS0_S0_S0_S0_S0_PfPKDF16_.kd
    .uniform_work_group_size: 1
    .uses_dynamic_stack: false
    .vgpr_count:     254
    .vgpr_spill_count: 0
    .wavefront_size: 64
  - .agpr_count:     0
    .args:
      - .actual_access:  read_only
        .address_space:  global
        .offset:         0
        .size:           8
        .value_kind:     global_buffer
      - .actual_access:  read_only
        .address_space:  global
        .offset:         8
        .size:           8
        .value_kind:     global_buffer
      - .actual_access:  read_only
        .address_space:  global
        .offset:         16
        .size:           8
        .value_kind:     global_buffer
      - .actual_access:  read_only
        .address_space:  global
        .offset:         24
        .size:           8
        .value_kind:     global_buffer
      - .actual_access:  read_only
        .address_space:  global
        .offset:         32
        .size:           8
        .value_kind:     global_buffer
      - .actual_access:  read_only
        .address_space:  global
        .offset:         40
        .size:           8
        .value_kind:     global_buffer
      - .actual_access:  read_only
        .address_space:  global
        .offset:         48
        .size:           8
        .value_kind:     global_buffer
      - .actual_access:  read_only
        .address_space:  global
        .offset:         56
        .size:           8
        .value_kind:     global_buffer
      - .actual_access:  read_only
        .address_space:  global
        .offset:         64
        .size:           8
        .value_kind:     global_buffer
      - .actual_access:  read_only
        .address_space:  global
        .offset:         72
        .size:           8
        .value_kind:     global_buffer
      - .actual_access:  write_only
        .address_space:  global
        .offset:         80
        .size:           8
        .value_kind:     global_buffer
    .group_segment_fixed_size: 70336
    .kernarg_segment_align: 8
    .kernarg_segment_size: 88
    .language:       OpenCL C
    .language_version:
      - 2
      - 0
    .max_flat_workgroup_size: 1024
    .name:           _Z13attend_kernelPKfS0_S0_S0_S0_S0_S0_S0_S0_S0_PDF16_
    .private_segment_fixed_size: 0
    .sgpr_count:     40
    .sgpr_spill_count: 0
    .symbol:         _Z13attend_kernelPKfS0_S0_S0_S0_S0_S0_S0_S0_S0_PDF16_.kd
    .uniform_work_group_size: 1
    .uses_dynamic_stack: false
    .vgpr_count:     86
    .vgpr_spill_count: 0
    .wavefront_size: 64
  - .agpr_count:     0
    .args:
      - .actual_access:  read_only
        .address_space:  global
        .offset:         0
        .size:           8
        .value_kind:     global_buffer
      - .actual_access:  read_only
        .address_space:  global
        .offset:         8
        .size:           8
        .value_kind:     global_buffer
      - .actual_access:  read_only
        .address_space:  global
        .offset:         16
        .size:           8
        .value_kind:     global_buffer
      - .actual_access:  read_only
        .address_space:  global
        .offset:         24
        .size:           8
        .value_kind:     global_buffer
      - .actual_access:  write_only
        .address_space:  global
        .offset:         32
        .size:           8
        .value_kind:     global_buffer
    .group_segment_fixed_size: 9088
    .kernarg_segment_align: 8
    .kernarg_segment_size: 40
    .language:       OpenCL C
    .language_version:
      - 2
      - 0
    .max_flat_workgroup_size: 512
    .name:           _Z16postfinal_kernelPKfS0_S0_S0_Pf
    .private_segment_fixed_size: 0
    .sgpr_count:     30
    .sgpr_spill_count: 0
    .symbol:         _Z16postfinal_kernelPKfS0_S0_S0_Pf.kd
    .uniform_work_group_size: 1
    .uses_dynamic_stack: false
    .vgpr_count:     124
    .vgpr_spill_count: 0
    .wavefront_size: 64
  - .agpr_count:     16
    .args:
      - .offset:         0
        .size:           1136
        .value_kind:     by_value
    .group_segment_fixed_size: 34816
    .kernarg_segment_align: 8
    .kernarg_segment_size: 1136
    .language:       OpenCL C
    .language_version:
      - 2
      - 0
    .max_flat_workgroup_size: 256
    .name:           _Z14gemm_nt_kernelILi2EEv8GemmArgs
    .private_segment_fixed_size: 0
    .sgpr_count:     68
    .sgpr_spill_count: 0
    .symbol:         _Z14gemm_nt_kernelILi2EEv8GemmArgs.kd
    .uniform_work_group_size: 1
    .uses_dynamic_stack: false
    .vgpr_count:     140
    .vgpr_spill_count: 0
    .wavefront_size: 64
  - .agpr_count:     0
    .args:
      - .actual_access:  read_only
        .address_space:  global
        .offset:         0
        .size:           8
        .value_kind:     global_buffer
      - .offset:         8
        .size:           8
        .value_kind:     by_value
      - .actual_access:  read_only
        .address_space:  global
        .offset:         16
        .size:           8
        .value_kind:     global_buffer
      - .actual_access:  read_only
        .address_space:  global
        .offset:         24
        .size:           8
        .value_kind:     global_buffer
      - .actual_access:  read_only
        .address_space:  global
        .offset:         32
        .size:           8
        .value_kind:     global_buffer
      - .actual_access:  read_only
        .address_space:  global
        .offset:         40
        .size:           8
        .value_kind:     global_buffer
      - .actual_access:  write_only
        .address_space:  global
        .offset:         48
        .size:           8
        .value_kind:     global_buffer
      - .actual_access:  write_only
        .address_space:  global
        .offset:         56
        .size:           8
        .value_kind:     global_buffer
      - .offset:         64
        .size:           4
        .value_kind:     by_value
      - .offset:         72
        .size:           376
        .value_kind:     by_value
    .group_segment_fixed_size: 62720
    .kernarg_segment_align: 8
    .kernarg_segment_size: 448
    .language:       OpenCL C
    .language_version:
      - 2
      - 0
    .max_flat_workgroup_size: 512
    .name:           _Z15gru_mfma_kernelILi1EEvPKfmS1_S1_S1_S1_PfS2_i7PreArgs
    .private_segment_fixed_size: 0
    .sgpr_count:     36
    .sgpr_spill_count: 0
    .symbol:         _Z15gru_mfma_kernelILi1EEvPKfmS1_S1_S1_S1_PfS2_i7PreArgs.kd
    .uniform_work_group_size: 1
    .uses_dynamic_stack: false
    .vgpr_count:     192
    .vgpr_spill_count: 0
    .wavefront_size: 64
  - .agpr_count:     0
    .args:
      - .actual_access:  read_only
        .address_space:  global
        .offset:         0
        .size:           8
        .value_kind:     global_buffer
      - .offset:         8
        .size:           8
        .value_kind:     by_value
      - .actual_access:  read_only
        .address_space:  global
        .offset:         16
        .size:           8
        .value_kind:     global_buffer
      - .actual_access:  read_only
        .address_space:  global
        .offset:         24
        .size:           8
        .value_kind:     global_buffer
      - .actual_access:  read_only
        .address_space:  global
        .offset:         32
        .size:           8
        .value_kind:     global_buffer
      - .actual_access:  read_only
        .address_space:  global
        .offset:         40
        .size:           8
        .value_kind:     global_buffer
      - .actual_access:  write_only
        .address_space:  global
        .offset:         48
        .size:           8
        .value_kind:     global_buffer
      - .actual_access:  write_only
        .address_space:  global
        .offset:         56
        .size:           8
        .value_kind:     global_buffer
      - .offset:         64
        .size:           4
        .value_kind:     by_value
      - .offset:         72
        .size:           376
        .value_kind:     by_value
    .group_segment_fixed_size: 64480
    .kernarg_segment_align: 8
    .kernarg_segment_size: 448
    .language:       OpenCL C
    .language_version:
      - 2
      - 0
    .max_flat_workgroup_size: 512
    .name:           _Z15gru_mfma_kernelILi2EEvPKfmS1_S1_S1_S1_PfS2_i7PreArgs
    .private_segment_fixed_size: 0
    .sgpr_count:     50
    .sgpr_spill_count: 0
    .symbol:         _Z15gru_mfma_kernelILi2EEvPKfmS1_S1_S1_S1_PfS2_i7PreArgs.kd
    .uniform_work_group_size: 1
    .uses_dynamic_stack: false
    .vgpr_count:     210
    .vgpr_spill_count: 0
    .wavefront_size: 64
